# expert-down GEMM K loop: in the first K iteration after an epilogue the first two vmcnt waits allow the 8 epilogue stores to stay in flight (same loads complete)
# baseline (speedup 1.0000x reference)
; #define GAS __attribute__((address_space(1)))
; #define LAS __attribute__((address_space(3)))
; #define PHASE_FRAME() Frame F = F0; asm volatile("" : "+s"(F.ws), "+s"(F.ctl), "+s"(F.G), "+s"(F.bid), "+s"(F.lds)); \
;     F.ws = (GAS unsigned char*)(GAS unsigned char*)F.ws; F.ctl = (GAS unsigned*)(GAS unsigned*)F.ctl;     \
;     GAS unsigned char* ws = F.ws; (void)ws
; __device__ __forceinline__ void build_toff(Frame& F, int layer) {
;     LAS int* toff = (LAS int*)(F.lds + LDS_TAB);
;     if (threadIdx.x < 64) {
;         const GAS unsigned* cnt = F.ctl + CW_CNT + layer * 64; const int e = (int)threadIdx.x;
;         const int tiles = ((int)__hip_atomic_load(cnt + e, RLX_AGENT) + 255) >> 8; int incl = tiles;
; #pragma unroll
;         for (int o = 1; o < 64; o <<= 1) { const int up = __shfl_up(incl, o); if (e >= o) incl += up; }
;         toff[e] = incl - tiles;
;         if (e == 63) { toff[N_EXPERTS] = incl; toff[NEXP1] = incl + T / 256; } }
;     __syncthreads();
; }
; template <int layer>
; __device__ __forceinline__ void run_layer(const Frame& F0, const XcdBarrier& bar, const int lo, const int hi) {
;     ...
;         if (IN(pb + 9)) { PHASE_FRAME();
;             build_toff(F, layer);
;             {
;                 EpiDown<true> E{(GAS bf16_t*)(ws + WS_Y)};
;                 MoeSched<8, false, 1> S{(const LAS int*)(F.lds + LDS_TAB), F.ctl + CW_CNT + layer * 64, (const GAS char*)(ws + WS_HID), (const GAS char*)(ws + (MOE8 ? WS_WDN8 : WS_WDN)), nullptr, F.G, F.bid, nullptr, (const LAS int*)(F.lds + LDS_TAB + 512)}; S.build_units((LAS int*)(F.lds + LDS_TAB + 512));
.LBB0_1931:
	s_mov_b32 s98, 0
	s_cmp_lt_i32 s54, 10
	s_cselect_b64 s[4:5], -1, 0
	s_and_b64 s[0:1], s[4:5], s[6:7]
	s_andn2_b64 vcc, exec, s[0:1]
	s_cbranch_vccnz .LBB0_1969
	s_mov_b32 s16, 0
	s_mov_b64 s[10:11], s[52:53]
	v_readlane_b32 s17, v254, 0
	s_mov_b64 s[8:9], s[52:53]
	s_mov_b32 s18, s95
	v_cmp_gt_u32_e32 vcc, 64, v0
	s_and_saveexec_b64 s[6:7], vcc
	s_cbranch_execz .LBB0_1935
	s_waitcnt vmcnt(15)
	v_lshlrev_b32_e32 v2, 2, v0
	v_mov_b32_e32 v3, 0
	v_lshl_add_u64 v[4:5], s[10:11], 0, v[2:3]
	v_add_co_u32_e32 v4, vcc, 0x1000, v4
	v_mbcnt_lo_u32_b32 v3, -1, 0
	s_nop 0
	v_addc_co_u32_e32 v5, vcc, 0, v5, vcc
	global_load_dword v1, v[4:5], off sc1
	v_mbcnt_hi_u32_b32 v3, -1, v3
	v_and_b32_e32 v4, 64, v3
	v_add_u32_e32 v5, -1, v3
	v_cmp_lt_i32_e32 vcc, v5, v4
	s_waitcnt vmcnt(15)
	v_add_u32_e32 v6, -2, v3
	v_readlane_b32 s0, v254, 3
	v_cndmask_b32_e32 v5, v5, v3, vcc
	v_lshlrev_b32_e32 v5, 2, v5
	v_cmp_lt_i32_e32 vcc, v6, v4
	v_readlane_b32 s1, v254, 4
	v_add_u32_e32 v7, -4, v3
	v_cndmask_b32_e32 v6, v6, v3, vcc
	v_lshlrev_b32_e32 v6, 2, v6
	v_cmp_lt_i32_e32 vcc, v7, v4
	v_add_u32_e32 v8, -8, v3
	v_add_u32_e32 v9, -16, v3
	v_cndmask_b32_e32 v7, v7, v3, vcc
	v_cmp_lt_u32_e32 vcc, 1, v0
	v_lshlrev_b32_e32 v7, 2, v7
	v_add_u32_e32 v2, s16, v2
	v_add_u32_e32 v2, 0x24000, v2
	s_waitcnt vmcnt(0)
	v_add_u32_e32 v1, 0xff, v1
	v_ashrrev_i32_e32 v10, 8, v1
	ds_bpermute_b32 v1, v5, v10
	v_subrev_u32_e32 v5, 32, v3
	s_waitcnt lgkmcnt(0)
	v_cndmask_b32_e64 v1, v1, 0, s[0:1]
	v_add_u32_e32 v1, v1, v10
	ds_bpermute_b32 v6, v6, v1
	s_waitcnt lgkmcnt(0)
	v_cndmask_b32_e32 v6, 0, v6, vcc
	v_add_u32_e32 v1, v6, v1
	ds_bpermute_b32 v6, v7, v1
	v_cmp_lt_i32_e32 vcc, v8, v4
	s_nop 1
	v_cndmask_b32_e32 v7, v8, v3, vcc
	v_cmp_lt_u32_e32 vcc, 3, v0
	v_lshlrev_b32_e32 v7, 2, v7
	s_waitcnt lgkmcnt(0)
	v_cndmask_b32_e32 v6, 0, v6, vcc
	v_add_u32_e32 v1, v6, v1
	ds_bpermute_b32 v6, v7, v1
	v_cmp_lt_i32_e32 vcc, v9, v4
	s_nop 1
	v_cndmask_b32_e32 v7, v9, v3, vcc
	v_cmp_lt_u32_e32 vcc, 7, v0
	v_lshlrev_b32_e32 v7, 2, v7
	s_waitcnt lgkmcnt(0)
	v_cndmask_b32_e32 v6, 0, v6, vcc
	v_add_u32_e32 v1, v6, v1
	ds_bpermute_b32 v6, v7, v1
	v_cmp_lt_i32_e32 vcc, v5, v4
	s_nop 1
	v_cndmask_b32_e32 v3, v5, v3, vcc
	v_cmp_lt_u32_e32 vcc, 15, v0
	v_lshlrev_b32_e32 v3, 2, v3
	s_waitcnt lgkmcnt(0)
	v_cndmask_b32_e32 v4, 0, v6, vcc
	v_add_u32_e32 v1, v4, v1
	ds_bpermute_b32 v3, v3, v1
	v_cmp_lt_u32_e32 vcc, 31, v0
	s_waitcnt lgkmcnt(0)
	s_nop 0
	v_cndmask_b32_e32 v3, 0, v3, vcc
	v_add_u32_e32 v1, v3, v1
	v_sub_u32_e32 v3, v1, v10
	v_cmp_eq_u32_e32 vcc, 63, v0
	ds_write_b32 v2, v3
	s_and_b64 exec, exec, vcc
	s_add_i32 s0, s16, 0x24100
	v_add_u32_e32 v2, 64, v1
	v_mov_b32_e32 v3, s0
	ds_write2_b32 v3, v1, v2 offset1:1

; #define GAS __attribute__((address_space(1)))
; #define PG8_STAGE(bufoff, gbase, voff) do { _Pragma("unroll") for (int _i = 0; _i < 2; ++_i) \
;         __builtin_amdgcn_global_load_lds((const GAS unsigned*)((const GAS char*)(gbase) + (voff)[_i]), (LAS unsigned*)(lds + (bufoff) + ldsw + _i * 8192), 16, 0, 0); } while (0)
; #define PG8_LDA(dst, b, h) do { _Pragma("unroll") for (int m = 0; m < 4; ++m) { dst[m].lo = *(const LAS i32x4v*)(lds + PG8_SA(b, h) + (FP8 ? aoff8[0] : aoff) + m * 2048); dst[m].hi = *(const LAS i32x4v*)(lds + PG8_SA(b, h) + (FP8 ? aoff8[1] : aoff + 1024) + m * 2048); } } while (0)
; #define PG8_LDB(dst, b, h) do { _Pragma("unroll") for (int n = 0; n < 2; ++n) { dst[n].lo = *(const LAS i32x4v*)(lds + PG8_SB(b, h) + (FP8 ? boff8[0] : boff) + n * 2048); dst[n].hi = *(const LAS i32x4v*)(lds + PG8_SB(b, h) + (FP8 ? boff8[1] : boff + 1024) + n * 2048); } } while (0)
; #define PG8_WAIT_V(n) asm volatile("s_waitcnt vmcnt(" #n ")" ::: "memory")
; template <class Epi, class Sched, bool GATHER, bool FP8 = false, bool UNI = false>
; __device__ __forceinline__ void gemm_phase(LAS unsigned char* lds, const Sched& S, const Epi& E) {
;     ...
;         for (int t = 0; t < nt; t += 2) {
;             const bool last = (t == nt - 2);
;             const GAS char* a1 = cA + (size_t)(t + 1) * 128;
;             const GAS char* a2 = last ? nA : cA + (size_t)(t + 2) * 128; const GAS char* b2 = last ? nB : cB + (size_t)(t + 2) * 128;
;             const GAS char* a3 = a2 + 128; const GAS char* b3 = b2 + 128;
;             const size_t hB2 = last ? hBn : hBc;
;             unsigned oa0[2], oa1[2], ob[2];
; #pragma unroll
;             for (int i = 0; i < 2; ++i) { if constexpr (UNI) { oa0[i] = aoc[0][i]; oa1[i] = aoc[1][i]; ob[i] = boc[i]; } else { oa0[i] = last ? aon[0][i] : aoc[0][i]; oa1[i] = last ? aon[1][i] : aoc[1][i]; ob[i] = last ? bon[i] : boc[i]; } }
;             PG8_LDB(B0, 0, 0); PG8_LDB(B1, 0, 1); PG8_SCHED; PG8_LDA(At, 0, 0); PG8_STAGE(PG8_SA(1, 1), a1, aoc[1]);
;             PG8_WAIT_V(8); PG8_WAIT_L(0); PG8_BAR; PG8_MMA(0, 0, At, B0); PG8_MMA(0, 1, At, B1); PG8_BAR; PG8_SCHED;
;             PG8_LDA(At, 0, 1); PG8_STAGE(PG8_SB(0, 0), b2, ob); PG8_STAGE(PG8_SB(0, 1), b2 + hB2, ob); PG8_STAGE(PG8_SA(0, 0), a2, oa0);
;             PG8_WAIT_V(8); PG8_WAIT_L(0); PG8_BAR; PG8_MMA(1, 0, At, B0); PG8_MMA(1, 1, At, B1); PG8_BAR; PG8_SCHED;
.LBB0_1961:
	s_add_u32 s40, s20, s36
	s_addc_u32 s41, s21, 0
	s_add_u32 s37, s40, 0x100
	s_addc_u32 s38, s41, 0
	s_and_b64 s[34:35], s[30:31], exec
	ds_read_b128 v[18:21], v1
	ds_read_b128 v[26:29], v1 offset:2048
	ds_read_b128 v[22:25], v186
	ds_read_b128 v[30:33], v186 offset:2048
	s_waitcnt lgkmcnt(0)
	ds_read_b128 v[2:5], v187
	ds_read_b128 v[10:13], v187 offset:2048
	ds_read_b128 v[6:9], v188
	ds_read_b128 v[14:17], v188 offset:2048
	s_cselect_b32 s34, s16, s37
	s_cselect_b32 s35, s17, s38
	s_add_u32 s36, s22, s36
	s_addc_u32 s37, s23, 0
	s_add_u32 s36, s36, 0x100
	s_addc_u32 s37, s37, 0
	s_and_b64 s[30:31], s[30:31], exec
	s_cselect_b32 s37, s19, s37
	s_cselect_b32 s36, s18, s36
	s_add_i32 m0, s45, 0xc000
	s_add_i32 s70, s45, 0xe000
	s_add_u32 s38, s36, 0x4000
	s_addc_u32 s39, s37, 0
	s_add_u32 s30, s36, 0x4080
	s_addc_u32 s31, s37, 0
	v_lshl_add_u64 v[224:225], s[40:41], 0, v[166:167]
	v_lshl_add_u64 v[224:225], v[224:225], 0, s[10:11]
	ds_read_b128 v[178:181], v189
	ds_read_b128 v[200:203], v189 offset:2048
	ds_read_b128 v[182:185], v190
	ds_read_b128 v[204:207], v190 offset:2048
	ds_read_b128 v[208:211], v189 offset:4096
	ds_read_b128 v[216:219], v189 offset:6144
	ds_read_b128 v[212:215], v190 offset:4096
	ds_read_b128 v[220:223], v190 offset:6144
	global_load_lds_dwordx4 v[224:225], off
	v_lshl_add_u64 v[224:225], s[40:41], 0, v[172:173]
	v_lshl_add_u64 v[224:225], v[224:225], 0, s[10:11]
	s_mov_b32 m0, s70
	s_nop 0
	global_load_lds_dwordx4 v[224:225], off
	s_and_b32 s99, s28, s98
	s_cbranch_scc1 .Lvw_p9a_0
	s_waitcnt vmcnt(8)
.Lvw_p9a_0:
	s_waitcnt vmcnt(16)
	s_waitcnt lgkmcnt(0)
	s_barrier
	s_setprio 1
	s_waitcnt lgkmcnt(0)
	v_mfma_scale_f32_16x16x128_f8f6f4 v[158:161], v[18:25], v[178:185], v[158:161], v191, v192 op_sel_hi:[0,0,0]
	v_mfma_scale_f32_16x16x128_f8f6f4 v[154:157], v[26:33], v[178:185], v[154:157], v191, v192 op_sel_hi:[0,0,0]
	v_mfma_scale_f32_16x16x128_f8f6f4 v[142:145], v[18:25], v[200:207], v[142:145], v191, v192 op_sel_hi:[0,0,0]
	v_mfma_scale_f32_16x16x128_f8f6f4 v[138:141], v[26:33], v[200:207], v[138:141], v191, v192 op_sel_hi:[0,0,0]
	v_mfma_scale_f32_16x16x128_f8f6f4 v[126:129], v[18:25], v[208:215], v[126:129], v191, v192 op_sel_hi:[0,0,0]
	v_mfma_scale_f32_16x16x128_f8f6f4 v[122:125], v[26:33], v[208:215], v[122:125], v191, v192 op_sel_hi:[0,0,0]
	v_mfma_scale_f32_16x16x128_f8f6f4 v[106:109], v[18:25], v[216:223], v[106:109], v191, v192 op_sel_hi:[0,0,0]
	v_mfma_scale_f32_16x16x128_f8f6f4 v[98:101], v[26:33], v[216:223], v[98:101], v191, v192 op_sel_hi:[0,0,0]
	s_setprio 0
	s_setprio 1
	v_mfma_scale_f32_16x16x128_f8f6f4 v[150:153], v[2:9], v[178:185], v[150:153], v191, v192 op_sel_hi:[0,0,0]
	v_mfma_scale_f32_16x16x128_f8f6f4 v[146:149], v[10:17], v[178:185], v[146:149], v191, v192 op_sel_hi:[0,0,0]
	v_mfma_scale_f32_16x16x128_f8f6f4 v[134:137], v[2:9], v[200:207], v[134:137], v191, v192 op_sel_hi:[0,0,0]
	v_mfma_scale_f32_16x16x128_f8f6f4 v[130:133], v[10:17], v[200:207], v[130:133], v191, v192 op_sel_hi:[0,0,0]
	v_mfma_scale_f32_16x16x128_f8f6f4 v[118:121], v[2:9], v[208:215], v[118:121], v191, v192 op_sel_hi:[0,0,0]
	v_mfma_scale_f32_16x16x128_f8f6f4 v[114:117], v[10:17], v[208:215], v[114:117], v191, v192 op_sel_hi:[0,0,0]
	v_mfma_scale_f32_16x16x128_f8f6f4 v[86:89], v[2:9], v[216:223], v[86:89], v191, v192 op_sel_hi:[0,0,0]
	v_mfma_scale_f32_16x16x128_f8f6f4 v[82:85], v[10:17], v[216:223], v[82:85], v191, v192 op_sel_hi:[0,0,0]
	s_setprio 0
	s_barrier
	s_mov_b32 m0, s33
	v_lshl_add_u64 v[178:179], s[36:37], 0, v[162:163]
	ds_read_b128 v[200:203], v189 offset:16384
	ds_read_b128 v[208:211], v189 offset:18432
	ds_read_b128 v[204:207], v190 offset:16384
	ds_read_b128 v[212:215], v190 offset:18432
	ds_read_b128 v[216:219], v189 offset:20480
	ds_read_b128 v[224:227], v189 offset:22528
	ds_read_b128 v[220:223], v190 offset:20480
	ds_read_b128 v[228:231], v190 offset:22528
	global_load_lds_dwordx4 v[178:179], off
	v_lshl_add_u64 v[180:181], s[36:37], 0, v[168:169]
	s_mov_b32 m0, s42
	v_lshl_add_u64 v[182:183], s[38:39], 0, v[162:163]
	global_load_lds_dwordx4 v[180:181], off
	s_mov_b32 m0, s43
	v_lshl_add_u64 v[184:185], s[34:35], 0, v[170:171]
	global_load_lds_dwordx4 v[182:183], off
	v_lshl_add_u64 v[182:183], s[38:39], 0, v[168:169]
	s_mov_b32 m0, s44
	s_nop 0
	global_load_lds_dwordx4 v[182:183], off
	v_lshl_add_u64 v[182:183], s[34:35], 0, v[164:165]
	s_mov_b32 m0, s45
	s_nop 0
	global_load_lds_dwordx4 v[182:183], off
	s_mov_b32 m0, s46
	s_nop 0
	global_load_lds_dwordx4 v[184:185], off
	s_and_b32 s99, s28, s98
	s_cbranch_scc1 .Lvw_p9a_1
	s_waitcnt vmcnt(8)
; #define PG8_STAGE(bufoff, gbase, voff) do { _Pragma("unroll") for (int _i = 0; _i < 2; ++_i) \
;         __builtin_amdgcn_global_load_lds((const GAS unsigned*)((const GAS char*)(gbase) + (voff)[_i]), (LAS unsigned*)(lds + (bufoff) + ldsw + _i * 8192), 16, 0, 0); } while (0)
; #define PG8_LDA(dst, b, h) do { _Pragma("unroll") for (int m = 0; m < 4; ++m) { dst[m].lo = *(const LAS i32x4v*)(lds + PG8_SA(b, h) + (FP8 ? aoff8[0] : aoff) + m * 2048); dst[m].hi = *(const LAS i32x4v*)(lds + PG8_SA(b, h) + (FP8 ? aoff8[1] : aoff + 1024) + m * 2048); } } while (0)
; #define PG8_LDB(dst, b, h) do { _Pragma("unroll") for (int n = 0; n < 2; ++n) { dst[n].lo = *(const LAS i32x4v*)(lds + PG8_SB(b, h) + (FP8 ? boff8[0] : boff) + n * 2048); dst[n].hi = *(const LAS i32x4v*)(lds + PG8_SB(b, h) + (FP8 ? boff8[1] : boff + 1024) + n * 2048); } } while (0)
; #define PG8_WAIT_V(n) asm volatile("s_waitcnt vmcnt(" #n ")" ::: "memory")
; #define PG8_WAIT_L(n) asm volatile("s_waitcnt lgkmcnt(" #n ")" ::: "memory")
; #define PG8_BAR __builtin_amdgcn_s_barrier()
; #define PG8_SCHED __builtin_amdgcn_sched_barrier(0)
; template <class Epi, class Sched, bool GATHER, bool FP8 = false, bool UNI = false>
; __device__ __forceinline__ void gemm_phase(LAS unsigned char* lds, const Sched& S, const Epi& E) {
;     ...
;             PG8_WAIT_V(8); PG8_WAIT_L(0); PG8_BAR; PG8_MMA(1, 0, At, B0); PG8_MMA(1, 1, At, B1); PG8_BAR; PG8_SCHED;
;             PG8_LDB(B0, 1, 0); PG8_LDB(B1, 1, 1); PG8_SCHED; PG8_LDA(At, 1, 0); PG8_STAGE(PG8_SA(0, 1), a2, oa1);
;             PG8_WAIT_V(8); PG8_WAIT_L(0); PG8_BAR; PG8_MMA(0, 0, At, B0); PG8_MMA(0, 1, At, B1); PG8_BAR; PG8_SCHED;
;             PG8_LDA(At, 1, 1); PG8_STAGE(PG8_SB(1, 0), b3, ob); PG8_STAGE(PG8_SB(1, 1), b3 + hB2, ob); PG8_STAGE(PG8_SA(1, 0), a3, oa0);
;             PG8_WAIT_V(8); PG8_WAIT_L(0); PG8_BAR; PG8_MMA(1, 0, At, B0); PG8_MMA(1, 1, At, B1); PG8_BAR; PG8_SCHED;
.Lvw_p9a_1:
	s_waitcnt vmcnt(16)
	s_waitcnt lgkmcnt(0)
	s_barrier
	s_setprio 1
	s_waitcnt lgkmcnt(0)
	v_mfma_scale_f32_16x16x128_f8f6f4 v[70:73], v[18:25], v[200:207], v[70:73], v191, v192 op_sel_hi:[0,0,0]
	v_mfma_scale_f32_16x16x128_f8f6f4 v[66:69], v[26:33], v[200:207], v[66:69], v191, v192 op_sel_hi:[0,0,0]
	v_mfma_scale_f32_16x16x128_f8f6f4 v[38:41], v[18:25], v[208:215], v[38:41], v191, v192 op_sel_hi:[0,0,0]
	v_mfma_scale_f32_16x16x128_f8f6f4 v[34:37], v[26:33], v[208:215], v[34:37], v191, v192 op_sel_hi:[0,0,0]
	v_mfma_scale_f32_16x16x128_f8f6f4 v[54:57], v[18:25], v[216:223], v[54:57], v191, v192 op_sel_hi:[0,0,0]
	v_mfma_scale_f32_16x16x128_f8f6f4 v[62:65], v[26:33], v[216:223], v[62:65], v191, v192 op_sel_hi:[0,0,0]
	v_mfma_scale_f32_16x16x128_f8f6f4 v[42:45], v[18:25], v[224:231], v[42:45], v191, v192 op_sel_hi:[0,0,0]
	v_mfma_scale_f32_16x16x128_f8f6f4 v[46:49], v[26:33], v[224:231], v[46:49], v191, v192 op_sel_hi:[0,0,0]
	s_setprio 0
	s_setprio 1
	v_mfma_scale_f32_16x16x128_f8f6f4 v[102:105], v[2:9], v[200:207], v[102:105], v191, v192 op_sel_hi:[0,0,0]
	v_mfma_scale_f32_16x16x128_f8f6f4 v[110:113], v[10:17], v[200:207], v[110:113], v191, v192 op_sel_hi:[0,0,0]
	v_mfma_scale_f32_16x16x128_f8f6f4 v[90:93], v[2:9], v[208:215], v[90:93], v191, v192 op_sel_hi:[0,0,0]
	v_mfma_scale_f32_16x16x128_f8f6f4 v[94:97], v[10:17], v[208:215], v[94:97], v191, v192 op_sel_hi:[0,0,0]
	v_mfma_scale_f32_16x16x128_f8f6f4 v[74:77], v[2:9], v[216:223], v[74:77], v191, v192 op_sel_hi:[0,0,0]
	v_mfma_scale_f32_16x16x128_f8f6f4 v[78:81], v[10:17], v[216:223], v[78:81], v191, v192 op_sel_hi:[0,0,0]
	v_mfma_scale_f32_16x16x128_f8f6f4 v[50:53], v[2:9], v[224:231], v[50:53], v191, v192 op_sel_hi:[0,0,0]
	v_mfma_scale_f32_16x16x128_f8f6f4 v[58:61], v[10:17], v[224:231], v[58:61], v191, v192 op_sel_hi:[0,0,0]
	s_setprio 0
	s_barrier
	ds_read_b128 v[2:5], v193
	ds_read_b128 v[10:13], v193 offset:2048
	ds_read_b128 v[6:9], v194
	ds_read_b128 v[14:17], v194 offset:2048
	ds_read_b128 v[18:21], v195
	ds_read_b128 v[26:29], v195 offset:2048
	ds_read_b128 v[22:25], v196
	ds_read_b128 v[30:33], v196 offset:2048
	s_mov_b32 m0, s47
	v_lshl_add_u64 v[232:233], s[34:35], 0, v[166:167]
	ds_read_b128 v[200:203], v189 offset:32768
	ds_read_b128 v[208:211], v189 offset:34816
	ds_read_b128 v[204:207], v190 offset:32768
	ds_read_b128 v[212:215], v190 offset:34816
	ds_read_b128 v[216:219], v189 offset:36864
	ds_read_b128 v[224:227], v189 offset:38912
	ds_read_b128 v[220:223], v190 offset:36864
	ds_read_b128 v[228:231], v190 offset:38912
	global_load_lds_dwordx4 v[232:233], off
	v_lshl_add_u64 v[232:233], s[34:35], 0, v[172:173]
	s_mov_b32 m0, s48
	s_nop 0
	global_load_lds_dwordx4 v[232:233], off
	s_waitcnt vmcnt(8)
	s_waitcnt lgkmcnt(0)
	s_barrier
	s_setprio 1
	s_waitcnt lgkmcnt(0)
	v_mfma_scale_f32_16x16x128_f8f6f4 v[158:161], v[2:9], v[200:207], v[158:161], v191, v192 op_sel_hi:[0,0,0]
	v_mfma_scale_f32_16x16x128_f8f6f4 v[154:157], v[10:17], v[200:207], v[154:157], v191, v192 op_sel_hi:[0,0,0]
	v_mfma_scale_f32_16x16x128_f8f6f4 v[142:145], v[2:9], v[208:215], v[142:145], v191, v192 op_sel_hi:[0,0,0]
	v_mfma_scale_f32_16x16x128_f8f6f4 v[138:141], v[10:17], v[208:215], v[138:141], v191, v192 op_sel_hi:[0,0,0]
	v_mfma_scale_f32_16x16x128_f8f6f4 v[126:129], v[2:9], v[216:223], v[126:129], v191, v192 op_sel_hi:[0,0,0]
	v_mfma_scale_f32_16x16x128_f8f6f4 v[122:125], v[10:17], v[216:223], v[122:125], v191, v192 op_sel_hi:[0,0,0]
	v_mfma_scale_f32_16x16x128_f8f6f4 v[106:109], v[2:9], v[224:231], v[106:109], v191, v192 op_sel_hi:[0,0,0]
	v_mfma_scale_f32_16x16x128_f8f6f4 v[98:101], v[10:17], v[224:231], v[98:101], v191, v192 op_sel_hi:[0,0,0]
	s_setprio 0
	s_setprio 1
	v_mfma_scale_f32_16x16x128_f8f6f4 v[150:153], v[18:25], v[200:207], v[150:153], v191, v192 op_sel_hi:[0,0,0]
	v_mfma_scale_f32_16x16x128_f8f6f4 v[146:149], v[26:33], v[200:207], v[146:149], v191, v192 op_sel_hi:[0,0,0]
	v_mfma_scale_f32_16x16x128_f8f6f4 v[134:137], v[18:25], v[208:215], v[134:137], v191, v192 op_sel_hi:[0,0,0]
	v_mfma_scale_f32_16x16x128_f8f6f4 v[130:133], v[26:33], v[208:215], v[130:133], v191, v192 op_sel_hi:[0,0,0]
	v_mfma_scale_f32_16x16x128_f8f6f4 v[118:121], v[18:25], v[216:223], v[118:121], v191, v192 op_sel_hi:[0,0,0]
	v_mfma_scale_f32_16x16x128_f8f6f4 v[114:117], v[26:33], v[216:223], v[114:117], v191, v192 op_sel_hi:[0,0,0]
	v_mfma_scale_f32_16x16x128_f8f6f4 v[86:89], v[18:25], v[224:231], v[86:89], v191, v192 op_sel_hi:[0,0,0]
	v_mfma_scale_f32_16x16x128_f8f6f4 v[82:85], v[26:33], v[224:231], v[82:85], v191, v192 op_sel_hi:[0,0,0]
	s_setprio 0
	s_barrier
	s_mov_b32 m0, s50
	v_lshl_add_u64 v[178:179], v[178:179], 0, s[10:11]
	ds_read_b128 v[200:203], v189 offset:49152
	ds_read_b128 v[208:211], v189 offset:51200
	ds_read_b128 v[204:207], v190 offset:49152
	ds_read_b128 v[212:215], v190 offset:51200
	ds_read_b128 v[216:219], v189 offset:53248
	ds_read_b128 v[224:227], v189 offset:55296
	ds_read_b128 v[220:223], v190 offset:53248
	ds_read_b128 v[228:231], v190 offset:55296
	global_load_lds_dwordx4 v[178:179], off
	v_lshl_add_u64 v[178:179], v[180:181], 0, s[10:11]
	s_mov_b32 m0, s51
	s_nop 0
	global_load_lds_dwordx4 v[178:179], off
	v_lshl_add_u64 v[178:179], s[30:31], 0, v[162:163]
	s_mov_b32 m0, s58
	s_nop 0
	global_load_lds_dwordx4 v[178:179], off
	v_lshl_add_u64 v[178:179], s[30:31], 0, v[168:169]
	s_mov_b32 m0, s59
	s_nop 0
	global_load_lds_dwordx4 v[178:179], off
	v_lshl_add_u64 v[178:179], v[182:183], 0, s[10:11]
	s_mov_b32 m0, s56
	s_nop 0
	global_load_lds_dwordx4 v[178:179], off
	v_lshl_add_u64 v[178:179], v[184:185], 0, s[10:11]
	s_mov_b32 m0, s57
	s_nop 0
	global_load_lds_dwordx4 v[178:179], off
	s_waitcnt vmcnt(8)
	s_waitcnt lgkmcnt(0)
	s_barrier
; #define PG8_WAIT_V(n) asm volatile("s_waitcnt vmcnt(" #n ")" ::: "memory")
; #define PG8_WAIT_L(n) asm volatile("s_waitcnt lgkmcnt(" #n ")" ::: "memory")
; #define PG8_BAR __builtin_amdgcn_s_barrier()
; #define PG8_SCHED __builtin_amdgcn_sched_barrier(0)
; template <class Epi, class Sched, bool GATHER, bool FP8 = false, bool UNI = false>
; __device__ __forceinline__ void gemm_phase(LAS unsigned char* lds, const Sched& S, const Epi& E) {
;     ...
;             PG8_WAIT_V(8); PG8_WAIT_L(0); PG8_BAR; PG8_MMA(1, 0, At, B0); PG8_MMA(1, 1, At, B1); PG8_BAR; PG8_SCHED;
;         }
;         if (wr == 0) PG8_BAR;
	s_setprio 1
	s_waitcnt lgkmcnt(0)
	v_mfma_scale_f32_16x16x128_f8f6f4 v[70:73], v[2:9], v[200:207], v[70:73], v191, v192 op_sel_hi:[0,0,0]
	v_mfma_scale_f32_16x16x128_f8f6f4 v[66:69], v[10:17], v[200:207], v[66:69], v191, v192 op_sel_hi:[0,0,0]
	v_mfma_scale_f32_16x16x128_f8f6f4 v[38:41], v[2:9], v[208:215], v[38:41], v191, v192 op_sel_hi:[0,0,0]
	v_mfma_scale_f32_16x16x128_f8f6f4 v[34:37], v[10:17], v[208:215], v[34:37], v191, v192 op_sel_hi:[0,0,0]
	v_mfma_scale_f32_16x16x128_f8f6f4 v[54:57], v[2:9], v[216:223], v[54:57], v191, v192 op_sel_hi:[0,0,0]
	v_mfma_scale_f32_16x16x128_f8f6f4 v[62:65], v[10:17], v[216:223], v[62:65], v191, v192 op_sel_hi:[0,0,0]
	v_mfma_scale_f32_16x16x128_f8f6f4 v[42:45], v[2:9], v[224:231], v[42:45], v191, v192 op_sel_hi:[0,0,0]
	v_mfma_scale_f32_16x16x128_f8f6f4 v[46:49], v[10:17], v[224:231], v[46:49], v191, v192 op_sel_hi:[0,0,0]
	s_setprio 0
	s_setprio 1
	v_mfma_scale_f32_16x16x128_f8f6f4 v[102:105], v[18:25], v[200:207], v[102:105], v191, v192 op_sel_hi:[0,0,0]
	v_mfma_scale_f32_16x16x128_f8f6f4 v[110:113], v[26:33], v[200:207], v[110:113], v191, v192 op_sel_hi:[0,0,0]
	v_mfma_scale_f32_16x16x128_f8f6f4 v[90:93], v[18:25], v[208:215], v[90:93], v191, v192 op_sel_hi:[0,0,0]
	v_mfma_scale_f32_16x16x128_f8f6f4 v[94:97], v[26:33], v[208:215], v[94:97], v191, v192 op_sel_hi:[0,0,0]
	v_mfma_scale_f32_16x16x128_f8f6f4 v[74:77], v[18:25], v[216:223], v[74:77], v191, v192 op_sel_hi:[0,0,0]
	v_mfma_scale_f32_16x16x128_f8f6f4 v[78:81], v[26:33], v[216:223], v[78:81], v191, v192 op_sel_hi:[0,0,0]
	v_mfma_scale_f32_16x16x128_f8f6f4 v[50:53], v[18:25], v[224:231], v[50:53], v191, v192 op_sel_hi:[0,0,0]
	v_mfma_scale_f32_16x16x128_f8f6f4 v[58:61], v[26:33], v[224:231], v[58:61], v191, v192 op_sel_hi:[0,0,0]
	s_setprio 0
	s_barrier
	s_movk_i32 s36, 0x100
	s_andn2_b64 vcc, exec, s[28:29]
	s_mov_b64 s[30:31], -1
	s_mov_b64 s[28:29], 0
	s_cbranch_vccz .LBB0_1961
	s_and_b64 vcc, exec, s[12:13]
	s_cbranch_vccz .LBB0_1964
	s_barrier
; #define GAS __attribute__((address_space(1)))
; #define LAS __attribute__((address_space(3)))
;     __device__ __forceinline__ bool operator()(f32x4 (&acc)[2][2][4][2], const Unit& u, int wr, int wc, int fr, int fq, LAS unsigned char* scr) const {
;         const int lane = fq * 16 + fr, rowb = u.row0 + wr * 64, colb = u.col0 + wc * 64;
; #pragma unroll
;         for (int ai = 0; ai < 2; ++ai)
; #pragma unroll
;             for (int m = 0; m < 4; ++m) { const size_t rg = (size_t)(rowb + ai * 128 + m * 16);
;                 if constexpr (F8OUT) {
;                     LAS unsigned char* sb = scr + ((ai * 4 + m) & 1) * 1024;
; #pragma unroll
;                     for (int bj = 0; bj < 2; ++bj) { const f32x4 v0 = acc[ai][bj][m][0], v1 = acc[ai][bj][m][1]; u32x2 w8;
;                         int q = __builtin_amdgcn_cvt_pk_fp8_f32(v0[0], v0[1], 0, false); q = __builtin_amdgcn_cvt_pk_fp8_f32(v0[2], v0[3], q, true); w8.x = (unsigned)q;
;                         q = __builtin_amdgcn_cvt_pk_fp8_f32(v1[0], v1[1], 0, false); q = __builtin_amdgcn_cvt_pk_fp8_f32(v1[2], v1[3], q, true); w8.y = (unsigned)q;
;                         *(LAS u32x2*)(sb + fr * 64 + bj * 32 + fq * 8) = w8; }
;                     const int r = lane >> 2, ch = lane & 3; const u32x4 o = *(const LAS u32x4*)(sb + r * 64 + ch * 16);
;                     *(GAS u32x4*)((GAS unsigned char*)Y + (rg + r) * D_MODEL + colb + ch * 16) = o;
.LBB0_1964:
	v_mov_b32_e32 v2, 0
	v_mov_b32_e32 v3, 0
	v_cvt_pk_fp8_f32 v2, v158, v159
	v_cvt_pk_fp8_f32 v3, v154, v155
	v_mov_b32_e32 v4, 0
	v_mov_b32_e32 v5, 0
	v_cvt_pk_fp8_f32 v4, v150, v151
	v_cvt_pk_fp8_f32 v5, v146, v147
	v_cvt_pk_fp8_f32 v2, v160, v161 op_sel:[0,0,1]
	v_cvt_pk_fp8_f32 v3, v156, v157 op_sel:[0,0,1]
	v_cvt_pk_fp8_f32 v4, v152, v153 op_sel:[0,0,1]
	v_cvt_pk_fp8_f32 v5, v148, v149 op_sel:[0,0,1]
	v_mov_b32_e32 v8, 0
	v_mov_b32_e32 v9, 0
	v_cvt_pk_fp8_f32 v8, v142, v143
	v_cvt_pk_fp8_f32 v9, v138, v139
	v_mov_b32_e32 v10, 0
	v_mov_b32_e32 v11, 0
	s_add_i32 s20, s69, s49
	v_cvt_pk_fp8_f32 v10, v134, v135
	v_cvt_pk_fp8_f32 v11, v130, v131
	ds_write_b64 v197, v[2:3]
	ds_write_b64 v255, v[4:5]
	s_ashr_i32 s21, s20, 31
	ds_read_b128 v[2:5], v198
	v_lshl_add_u64 v[6:7], s[20:21], 0, v[174:175]
	s_add_i32 s22, s68, s60
	v_lshlrev_b64 v[6:7], 11, v[6:7]
	v_cvt_pk_fp8_f32 v8, v144, v145 op_sel:[0,0,1]
	v_cvt_pk_fp8_f32 v9, v140, v141 op_sel:[0,0,1]
	s_ashr_i32 s23, s22, 31
	v_lshl_add_u64 v[6:7], s[8:9], 0, v[6:7]
	v_cvt_pk_fp8_f32 v10, v136, v137 op_sel:[0,0,1]
	v_cvt_pk_fp8_f32 v11, v132, v133 op_sel:[0,0,1]
	v_lshl_add_u64 v[6:7], v[6:7], 0, s[22:23]
	v_lshl_add_u64 v[12:13], v[6:7], 0, v[176:177]
	ds_write_b64 v197, v[8:9] offset:1024
	ds_write_b64 v255, v[10:11] offset:1024
	s_waitcnt lgkmcnt(0)
	global_store_dwordx4 v[12:13], v[2:5], off
	s_add_i32 s28, s20, 16
	v_mov_b32_e32 v10, 0
	v_mov_b32_e32 v4, 0
	v_mov_b32_e32 v5, 0
	v_cvt_pk_fp8_f32 v4, v126, v127
	v_cvt_pk_fp8_f32 v5, v122, v123
	v_mov_b32_e32 v11, 0
	s_ashr_i32 s29, s28, 31
	v_cvt_pk_fp8_f32 v10, v118, v119
	v_cvt_pk_fp8_f32 v11, v114, v115
	ds_read_b128 v[6:9], v198 offset:1024
	v_lshl_add_u64 v[2:3], s[28:29], 0, v[174:175]
	v_lshlrev_b64 v[2:3], 11, v[2:3]
	v_lshl_add_u64 v[2:3], s[8:9], 0, v[2:3]
	v_cvt_pk_fp8_f32 v4, v128, v129 op_sel:[0,0,1]
	v_cvt_pk_fp8_f32 v5, v124, v125 op_sel:[0,0,1]
	v_lshl_add_u64 v[2:3], v[2:3], 0, s[22:23]
	v_cvt_pk_fp8_f32 v10, v120, v121 op_sel:[0,0,1]
	v_cvt_pk_fp8_f32 v11, v116, v117 op_sel:[0,0,1]
	v_lshl_add_u64 v[2:3], v[2:3], 0, v[176:177]
	s_waitcnt lgkmcnt(0)
	global_store_dwordx4 v[2:3], v[6:9], off
	ds_write_b64 v197, v[4:5]
	ds_write_b64 v255, v[10:11]
	v_mov_b32_e32 v8, 0
	v_mov_b32_e32 v9, 0
	v_cvt_pk_fp8_f32 v8, v106, v107
	v_cvt_pk_fp8_f32 v9, v98, v99
	v_mov_b32_e32 v10, 0
	v_mov_b32_e32 v11, 0
	s_add_i32 s28, s20, 32
	v_cvt_pk_fp8_f32 v10, v86, v87
	v_cvt_pk_fp8_f32 v11, v82, v83
	s_ashr_i32 s29, s28, 31
	ds_read_b128 v[2:5], v198
	v_lshl_add_u64 v[6:7], s[28:29], 0, v[174:175]
	v_lshlrev_b64 v[6:7], 11, v[6:7]
	v_cvt_pk_fp8_f32 v8, v108, v109 op_sel:[0,0,1]
	v_cvt_pk_fp8_f32 v9, v100, v101 op_sel:[0,0,1]
	v_lshl_add_u64 v[6:7], s[8:9], 0, v[6:7]
	v_cvt_pk_fp8_f32 v10, v88, v89 op_sel:[0,0,1]
	v_cvt_pk_fp8_f32 v11, v84, v85 op_sel:[0,0,1]
	v_lshl_add_u64 v[6:7], v[6:7], 0, s[22:23]
	v_lshl_add_u64 v[12:13], v[6:7], 0, v[176:177]
	ds_write_b64 v197, v[8:9] offset:1024
	ds_write_b64 v255, v[10:11] offset:1024
	s_waitcnt lgkmcnt(0)
	global_store_dwordx4 v[12:13], v[2:5], off
	s_add_i32 s28, s20, 48
	v_mov_b32_e32 v10, 0
	v_mov_b32_e32 v4, 0
	v_mov_b32_e32 v5, 0
	v_cvt_pk_fp8_f32 v4, v70, v71
	v_cvt_pk_fp8_f32 v5, v66, v67
	v_mov_b32_e32 v11, 0
	s_ashr_i32 s29, s28, 31
	v_cvt_pk_fp8_f32 v10, v102, v103
	v_cvt_pk_fp8_f32 v11, v110, v111
	ds_read_b128 v[6:9], v198 offset:1024
	v_lshl_add_u64 v[2:3], s[28:29], 0, v[174:175]
	v_lshlrev_b64 v[2:3], 11, v[2:3]
	v_lshl_add_u64 v[2:3], s[8:9], 0, v[2:3]
	v_cvt_pk_fp8_f32 v4, v72, v73 op_sel:[0,0,1]
	v_cvt_pk_fp8_f32 v5, v68, v69 op_sel:[0,0,1]
	v_lshl_add_u64 v[2:3], v[2:3], 0, s[22:23]
	v_cvt_pk_fp8_f32 v10, v104, v105 op_sel:[0,0,1]
	v_cvt_pk_fp8_f32 v11, v112, v113 op_sel:[0,0,1]
	v_lshl_add_u64 v[2:3], v[2:3], 0, v[176:177]
	s_waitcnt lgkmcnt(0)
	global_store_dwordx4 v[2:3], v[6:9], off
	ds_write_b64 v197, v[4:5]
	ds_write_b64 v255, v[10:11]
	v_mov_b32_e32 v8, 0
	v_mov_b32_e32 v9, 0
	v_cvt_pk_fp8_f32 v8, v38, v39
	v_cvt_pk_fp8_f32 v9, v34, v35
	v_mov_b32_e32 v10, 0
	v_mov_b32_e32 v11, 0
	s_add_i32 s28, s20, 0x80
	v_cvt_pk_fp8_f32 v10, v90, v91
	v_cvt_pk_fp8_f32 v11, v94, v95
	s_ashr_i32 s29, s28, 31
	ds_read_b128 v[2:5], v198
	v_lshl_add_u64 v[6:7], s[28:29], 0, v[174:175]
	v_lshlrev_b64 v[6:7], 11, v[6:7]
	v_cvt_pk_fp8_f32 v8, v40, v41 op_sel:[0,0,1]
	v_cvt_pk_fp8_f32 v9, v36, v37 op_sel:[0,0,1]
	v_lshl_add_u64 v[6:7], s[8:9], 0, v[6:7]
	v_cvt_pk_fp8_f32 v10, v92, v93 op_sel:[0,0,1]
	v_cvt_pk_fp8_f32 v11, v96, v97 op_sel:[0,0,1]
	v_lshl_add_u64 v[6:7], v[6:7], 0, s[22:23]
	v_lshl_add_u64 v[12:13], v[6:7], 0, v[176:177]
	ds_write_b64 v197, v[8:9] offset:1024
	ds_write_b64 v255, v[10:11] offset:1024
	s_waitcnt lgkmcnt(0)
	global_store_dwordx4 v[12:13], v[2:5], off
	s_add_i32 s28, s20, 0x90
	v_mov_b32_e32 v10, 0
	v_mov_b32_e32 v4, 0
	v_mov_b32_e32 v5, 0
	v_cvt_pk_fp8_f32 v4, v54, v55
	v_cvt_pk_fp8_f32 v5, v62, v63
	v_mov_b32_e32 v11, 0
	s_ashr_i32 s29, s28, 31
	v_cvt_pk_fp8_f32 v10, v74, v75
	v_cvt_pk_fp8_f32 v11, v78, v79
	ds_read_b128 v[6:9], v198 offset:1024
	v_lshl_add_u64 v[2:3], s[28:29], 0, v[174:175]
	v_lshlrev_b64 v[2:3], 11, v[2:3]
	v_lshl_add_u64 v[2:3], s[8:9], 0, v[2:3]
	v_cvt_pk_fp8_f32 v4, v56, v57 op_sel:[0,0,1]
	v_cvt_pk_fp8_f32 v5, v64, v65 op_sel:[0,0,1]
	v_lshl_add_u64 v[2:3], v[2:3], 0, s[22:23]
	v_cvt_pk_fp8_f32 v10, v76, v77 op_sel:[0,0,1]
	v_cvt_pk_fp8_f32 v11, v80, v81 op_sel:[0,0,1]
	v_lshl_add_u64 v[2:3], v[2:3], 0, v[176:177]
	s_waitcnt lgkmcnt(0)
	global_store_dwordx4 v[2:3], v[6:9], off
	ds_write_b64 v197, v[4:5]
	ds_write_b64 v255, v[10:11]
	v_mov_b32_e32 v8, 0
	v_mov_b32_e32 v9, 0
	v_cvt_pk_fp8_f32 v8, v42, v43
	v_cvt_pk_fp8_f32 v9, v46, v47
	v_mov_b32_e32 v10, 0
	v_mov_b32_e32 v11, 0
	v_cvt_pk_fp8_f32 v10, v50, v51
	v_cvt_pk_fp8_f32 v11, v58, v59
	s_add_i32 s28, s20, 0xa0
	s_ashr_i32 s29, s28, 31
	ds_read_b128 v[2:5], v198
	v_lshl_add_u64 v[6:7], s[28:29], 0, v[174:175]
	v_cvt_pk_fp8_f32 v8, v44, v45 op_sel:[0,0,1]
	v_cvt_pk_fp8_f32 v9, v48, v49 op_sel:[0,0,1]
	v_lshlrev_b64 v[6:7], 11, v[6:7]
	v_cvt_pk_fp8_f32 v10, v52, v53 op_sel:[0,0,1]
	v_cvt_pk_fp8_f32 v11, v60, v61 op_sel:[0,0,1]
	v_lshl_add_u64 v[6:7], s[8:9], 0, v[6:7]
	v_lshl_add_u64 v[6:7], v[6:7], 0, s[22:23]
	s_addk_i32 s20, 0xb0
	v_lshl_add_u64 v[12:13], v[6:7], 0, v[176:177]
	ds_write_b64 v197, v[8:9] offset:1024
	ds_write_b64 v255, v[10:11] offset:1024
	s_ashr_i32 s21, s20, 31
	ds_read_b128 v[6:9], v198 offset:1024
	s_waitcnt lgkmcnt(0)
	global_store_dwordx4 v[12:13], v[2:5], off
	s_andn2_b64 vcc, exec, s[26:27]
	s_nop 0
	v_lshl_add_u64 v[2:3], s[20:21], 0, v[174:175]
	v_lshlrev_b64 v[2:3], 11, v[2:3]
	v_lshl_add_u64 v[2:3], s[8:9], 0, v[2:3]
	v_lshl_add_u64 v[2:3], v[2:3], 0, s[22:23]
	v_lshl_add_u64 v[2:3], v[2:3], 0, v[176:177]
	s_mov_b64 s[20:21], -1
	global_store_dwordx4 v[2:3], v[6:9], off
	s_mov_b32 s98, 1
	s_cbranch_vccnz .LBB0_1946
	s_andn2_b64 vcc, exec, s[6:7]
	s_cbranch_vccnz .LBB0_1945
	s_barrier
	s_branch .LBB0_1945

; #define GAS __attribute__((address_space(1)))
; #define LAS __attribute__((address_space(3)))
; #define PHASE_FRAME() Frame F = F0; asm volatile("" : "+s"(F.ws), "+s"(F.ctl), "+s"(F.G), "+s"(F.bid), "+s"(F.lds)); \
;     F.ws = (GAS unsigned char*)(GAS unsigned char*)F.ws; F.ctl = (GAS unsigned*)(GAS unsigned*)F.ctl;     \
;     GAS unsigned char* ws = F.ws; (void)ws
; __device__ __forceinline__ void build_toff(Frame& F, int layer) {
;     LAS int* toff = (LAS int*)(F.lds + LDS_TAB);
;     if (threadIdx.x < 64) {
;         const GAS unsigned* cnt = F.ctl + CW_CNT + layer * 64; const int e = (int)threadIdx.x;
;         const int tiles = ((int)__hip_atomic_load(cnt + e, RLX_AGENT) + 255) >> 8; int incl = tiles;
; #pragma unroll
;         for (int o = 1; o < 64; o <<= 1) { const int up = __shfl_up(incl, o); if (e >= o) incl += up; }
;         toff[e] = incl - tiles;
;         if (e == 63) { toff[N_EXPERTS] = incl; toff[NEXP1] = incl + T / 256; } }
;     __syncthreads();
; }
; template <int layer>
; __device__ __forceinline__ void run_layer(const Frame& F0, const XcdBarrier& bar, const int lo, const int hi) {
;     ...
;         if (IN(pb + 9)) { PHASE_FRAME();
;             build_toff(F, layer);
;             {
;                 EpiDown<true> E{(GAS bf16_t*)(ws + WS_Y)};
;                 MoeSched<8, false, 1> S{(const LAS int*)(F.lds + LDS_TAB), F.ctl + CW_CNT + layer * 64, (const GAS char*)(ws + WS_HID), (const GAS char*)(ws + (MOE8 ? WS_WDN8 : WS_WDN)), nullptr, F.G, F.bid, nullptr, (const LAS int*)(F.lds + LDS_TAB + 512)}; S.build_units((LAS int*)(F.lds + LDS_TAB + 512));
.LBB0_3159:
	s_mov_b32 s98, 0
	s_cmp_lt_i32 s54, 21
	s_cselect_b64 s[4:5], -1, 0
	s_and_b64 s[0:1], s[4:5], s[6:7]
	s_andn2_b64 vcc, exec, s[0:1]
	s_cbranch_vccnz .LBB0_3197
	s_mov_b32 s16, 0
	s_mov_b32 s17, s95
	s_mov_b64 s[10:11], s[52:53]
	v_readlane_b32 s18, v254, 0
	s_mov_b64 s[8:9], s[52:53]
	v_cmp_gt_u32_e32 vcc, 64, v0
	s_and_saveexec_b64 s[6:7], vcc
	s_cbranch_execz .LBB0_3163
	s_waitcnt vmcnt(0)
	v_lshlrev_b32_e32 v2, 2, v0
	v_mov_b32_e32 v3, 0
	v_lshl_add_u64 v[4:5], s[10:11], 0, v[2:3]
	v_add_co_u32_e32 v4, vcc, 0x1000, v4
	v_mbcnt_lo_u32_b32 v3, -1, 0
	s_nop 0
	v_addc_co_u32_e32 v5, vcc, 0, v5, vcc
	global_load_dword v1, v[4:5], off offset:256 sc1
	v_mbcnt_hi_u32_b32 v3, -1, v3
	v_and_b32_e32 v4, 64, v3
	v_add_u32_e32 v5, -1, v3
	v_cmp_lt_i32_e32 vcc, v5, v4
	v_add_u32_e32 v6, -2, v3
	v_readlane_b32 s0, v254, 3
	v_cndmask_b32_e32 v5, v5, v3, vcc
	v_lshlrev_b32_e32 v5, 2, v5
	v_cmp_lt_i32_e32 vcc, v6, v4
	v_readlane_b32 s1, v254, 4
	v_add_u32_e32 v7, -4, v3
	v_cndmask_b32_e32 v6, v6, v3, vcc
	v_lshlrev_b32_e32 v6, 2, v6
	v_cmp_lt_i32_e32 vcc, v7, v4
	v_add_u32_e32 v8, -8, v3
	v_add_u32_e32 v9, -16, v3
	v_cndmask_b32_e32 v7, v7, v3, vcc
	v_cmp_lt_u32_e32 vcc, 1, v0
	v_lshlrev_b32_e32 v7, 2, v7
	v_add_u32_e32 v2, s16, v2
	v_add_u32_e32 v2, 0x24000, v2
	s_waitcnt vmcnt(0)
	v_add_u32_e32 v1, 0xff, v1
	v_ashrrev_i32_e32 v10, 8, v1
	ds_bpermute_b32 v1, v5, v10
	v_subrev_u32_e32 v5, 32, v3
	s_waitcnt lgkmcnt(0)
	v_cndmask_b32_e64 v1, v1, 0, s[0:1]
	v_add_u32_e32 v1, v1, v10
	ds_bpermute_b32 v6, v6, v1
	s_waitcnt lgkmcnt(0)
	v_cndmask_b32_e32 v6, 0, v6, vcc
	v_add_u32_e32 v1, v6, v1
	ds_bpermute_b32 v6, v7, v1
	v_cmp_lt_i32_e32 vcc, v8, v4
	s_nop 1
	v_cndmask_b32_e32 v7, v8, v3, vcc
	v_cmp_lt_u32_e32 vcc, 3, v0
	v_lshlrev_b32_e32 v7, 2, v7
	s_waitcnt lgkmcnt(0)
	v_cndmask_b32_e32 v6, 0, v6, vcc
	v_add_u32_e32 v1, v6, v1
	ds_bpermute_b32 v6, v7, v1
	v_cmp_lt_i32_e32 vcc, v9, v4
	s_nop 1
	v_cndmask_b32_e32 v7, v9, v3, vcc
	v_cmp_lt_u32_e32 vcc, 7, v0
	v_lshlrev_b32_e32 v7, 2, v7
	s_waitcnt lgkmcnt(0)
	v_cndmask_b32_e32 v6, 0, v6, vcc
	v_add_u32_e32 v1, v6, v1
	ds_bpermute_b32 v6, v7, v1
	v_cmp_lt_i32_e32 vcc, v5, v4
	s_nop 1
	v_cndmask_b32_e32 v3, v5, v3, vcc
	v_cmp_lt_u32_e32 vcc, 15, v0
	v_lshlrev_b32_e32 v3, 2, v3
	s_waitcnt lgkmcnt(0)
	v_cndmask_b32_e32 v4, 0, v6, vcc
	v_add_u32_e32 v1, v4, v1
	ds_bpermute_b32 v3, v3, v1
	v_cmp_lt_u32_e32 vcc, 31, v0
	s_waitcnt lgkmcnt(0)
	s_nop 0
	v_cndmask_b32_e32 v3, 0, v3, vcc
	v_add_u32_e32 v1, v3, v1
	v_sub_u32_e32 v3, v1, v10
	v_cmp_eq_u32_e32 vcc, 63, v0
	ds_write_b32 v2, v3
	s_and_b64 exec, exec, vcc
	s_add_i32 s0, s16, 0x24100
	v_add_u32_e32 v2, 64, v1
	v_mov_b32_e32 v3, s0
	ds_write2_b32 v3, v1, v2 offset1:1
